# hybrid K1 ring 16 (14 private 16KiB chunks + queues) + last-chunk early flush
# speedup vs baseline: 1.0969x; 1.0592x over previous
.Lk1_scan:
	s_load_dwordx2 s[4:5], s[0:1], 0x0
	s_load_dwordx4 s[8:11], s[0:1], 0x20
	s_load_dwordx2 s[12:13], s[0:1], 0x30
	v_and_b32_e32 v6, 63, v0
	v_readfirstlane_b32 s3, v0
	v_lshlrev_b32_e32 v1, 4, v6
	v_lshlrev_b32_e32 v2, 2, v6
	v_or_b32_e32 v3, 1, v2
	v_or_b32_e32 v4, 2, v2
	v_or_b32_e32 v5, 3, v2
	s_lshr_b32 s3, s3, 6
	s_sub_u32 s16, s2, 0x60
	s_lshl_b32 s16, s16, 2
	s_add_u32 s16, s16, s3
	s_mul_i32 s17, s16, 0x48000
	s_lshr_b32 s18, s17, 2
	s_lshl_b32 s24, s3, 13
	s_mov_b32 s25, s24
	s_mov_b32 s28, s24
	s_mov_b32 s36, 0
	s_mov_b64 s[62:63], 0
	v_mov_b32_e32 v21, 1
	s_mov_b32 s27, 0
	s_mov_b32 s29, 0x55555556
	s_mov_b32 s31, 0xc0000
	s_waitcnt lgkmcnt(0)
	s_and_b32 s50, s16, 15
	s_mul_i32 s52, s50, 512
	s_add_u32 s52, s52, 28672
	s_lshl_b32 s53, s50, 6
	s_add_u32 s53, s53, 0xe000
	s_add_u32 s54, s10, s53
	s_addc_u32 s55, s11, 0
	s_mul_i32 s59, s16, 14
	s_mul_i32 s57, s59, 0x4000
	s_lshr_b32 s18, s57, 2
	s_add_u32 s6, s4, s57
	s_addc_u32 s7, s5, 0
	v_mov_b32_e32 v27, 0
	global_load_dwordx4 v[28:31], v1, s[6:7] nt
	s_add_u32 s6, s6, 0x400
	s_addc_u32 s7, s7, 0
	global_load_dwordx4 v[32:35], v1, s[6:7] nt
	s_add_u32 s6, s6, 0x400
	s_addc_u32 s7, s7, 0
	global_load_dwordx4 v[36:39], v1, s[6:7] nt
	s_add_u32 s6, s6, 0x400
	s_addc_u32 s7, s7, 0
	global_load_dwordx4 v[40:43], v1, s[6:7] nt
	s_add_u32 s6, s6, 0x400
	s_addc_u32 s7, s7, 0
	global_load_dwordx4 v[44:47], v1, s[6:7] nt
	s_add_u32 s6, s6, 0x400
	s_addc_u32 s7, s7, 0
	global_load_dwordx4 v[48:51], v1, s[6:7] nt
	s_add_u32 s6, s6, 0x400
	s_addc_u32 s7, s7, 0
	global_load_dwordx4 v[52:55], v1, s[6:7] nt
	s_add_u32 s6, s6, 0x400
	s_addc_u32 s7, s7, 0
	global_load_dwordx4 v[56:59], v1, s[6:7] nt
	s_add_u32 s6, s6, 0x400
	s_addc_u32 s7, s7, 0
	global_load_dwordx4 v[60:63], v1, s[6:7] nt
	s_add_u32 s6, s6, 0x400
	s_addc_u32 s7, s7, 0
	global_load_dwordx4 v[64:67], v1, s[6:7] nt
	s_add_u32 s6, s6, 0x400
	s_addc_u32 s7, s7, 0
	global_load_dwordx4 v[68:71], v1, s[6:7] nt
	s_add_u32 s6, s6, 0x400
	s_addc_u32 s7, s7, 0
	global_load_dwordx4 v[72:75], v1, s[6:7] nt
	s_add_u32 s6, s6, 0x400
	s_addc_u32 s7, s7, 0
	global_load_dwordx4 v[76:79], v1, s[6:7] nt
	s_add_u32 s6, s6, 0x400
	s_addc_u32 s7, s7, 0
	global_load_dwordx4 v[80:83], v1, s[6:7] nt
	s_add_u32 s6, s6, 0x400
	s_addc_u32 s7, s7, 0
	global_load_dwordx4 v[84:87], v1, s[6:7] nt
	s_add_u32 s6, s6, 0x400
	s_addc_u32 s7, s7, 0
	global_load_dwordx4 v[88:91], v1, s[6:7] nt
	s_add_u32 s6, s6, 0x400
	s_addc_u32 s7, s7, 0
	s_mov_b32 s26, 18
	s_add_u32 s57, s59, 1
	s_mul_i32 s57, s57, 0x4000
	s_lshr_b32 s58, s57, 2
	s_add_u32 s6, s4, s57
	s_addc_u32 s7, s5, 0
	s_mov_b32 s26, 0

.Lk1_inone_l:
	s_cmp_ge_u32 s28, s25
	s_cbranch_scc1 .Lk1_inone_lx
	s_waitcnt lgkmcnt(0)
	v_lshl_add_u32 v25, v6, 3, s28
	v_cmp_gt_u32_e32 vcc, s25, v25
	s_and_saveexec_b64 s[32:33], vcc
	s_mov_b64 s[62:63], exec
	ds_read_b64 v[92:93], v25
	s_waitcnt lgkmcnt(0)
	v_lshrrev_b32_e32 v97, 12, v92
	v_mul_hi_u32 v97, v97, s29
	v_mul_u32_u24_e32 v94, 0x3000, v97
	v_sub_u32_e32 v94, v92, v94
	v_lshlrev_b32_e32 v95, 2, v94
	global_atomic_add v96, v95, v21, s[8:9] sc0
	global_atomic_add_f32 v95, v93, s[10:11]
	v_mov_b32_e32 v92, v97
	s_mov_b64 exec, -1
	s_add_u32 s28, s28, 0x200
	s_cmp_ge_u32 s28, s25
	s_cbranch_scc0 .Lk1_inone_lx
	s_mov_b32 s28, s24
	s_mov_b32 s25, s24

.Lk1_cskip_fin_pend:
	s_mov_b64 exec, s[62:63]
	s_cbranch_execz .Lk1_cskip_fin_x
	v_mul_u32_u24_e32 v98, 0x3000, v94
	v_lshlrev_b32_e32 v97, 6, v94
	v_cmp_gt_u32_e32 vcc, 64, v96
	v_add_u32_e32 v97, v97, v96
	v_add3_u32 v98, v98, v96, s31
	v_cndmask_b32_e32 v97, v98, v97, vcc
	v_lshlrev_b32_e32 v97, 3, v97
	global_store_dwordx2 v97, v[92:93], s[12:13]
